# v17
# speedup vs baseline: 1.0210x; 1.0012x over previous
.LBB1_3:
	v_lshrrev_b32_e32 v3, 4, v0
	v_and_b32_e32 v4, 15, v0
	v_bfe_u32 v5, v0, 4, 2
	v_and_b32_e32 v7, 7, v0
	s_lshl_b32 s0, s30, 5
	s_sext_i32_i16 s76, s28
	v_lshl_or_b32 v207, s31, 6, v4
	v_bitop3_b32 v3, v3, v7, 3 bitop3:0x6c
	v_bitop3_b32 v7, v5, v7, 4 bitop3:0x36
	s_and_b32 s28, s0, 0x60
	v_lshlrev_b32_e32 v6, 7, v207
	v_lshlrev_b32_e32 v3, 4, v3
	v_lshlrev_b32_e32 v7, 4, v7
	v_or_b32_e32 v4, s28, v4
	s_cmp_lg_u32 s16, 0
	v_lshlrev_b32_e32 v206, 2, v0
	v_lshlrev_b32_e32 v230, 4, v0
	v_lshlrev_b32_e32 v231, 3, v0
	v_lshlrev_b32_e32 v0, 4, v0
	v_or_b32_e32 v8, v6, v3
	v_or_b32_e32 v6, v6, v7
	v_lshlrev_b32_e32 v4, 7, v4
	s_cselect_b64 s[0:1], -1, 0
	v_add_u32_e32 v208, v2, v1
	v_add_u32_e32 v0, 0, v0
	v_or_b32_e32 v222, v4, v3
	v_or_b32_e32 v223, v4, v7
	v_add_u32_e32 v228, 0x10000, v222
	v_add_u32_e32 v229, 0x10000, v223
	s_mul_i32 s65, s2, 0x70
	v_lshl_or_b32 v224, v5, 3, s28
	v_add_u32_e32 v210, 0x80000, v208
	v_mov_b32_e32 v211, v205
	v_mov_b32_e32 v209, v205
	s_and_b64 s[0:1], exec, s[0:1]
	s_movk_i32 s16, 0xe00
	v_add_u32_e32 v225, 0x20000, v0
	s_add_i32 s66, 0, 0x10000
	s_add_i32 s67, 0, 0x10800
	s_add_i32 s68, 0, 0x14000
	s_add_i32 s69, 0, 0x14800
	s_add_i32 s70, 0, 0x18000
	s_add_i32 s71, 0, 0x18800
	s_add_i32 s72, 0, 0x1c000
	s_add_i32 s73, 0, 0x1c800
	s_movk_i32 s74, 0x7000
	v_add_u32_e32 v226, 0, v8
	v_add_u32_e32 v227, 0, v6
	s_mov_b32 s30, s29
	s_mov_b32 s34, s29
	s_mov_b32 s28, 0
	s_branch .LBB1_5

.LBB1_9:
	s_add_i32 s82, s48, 2
	s_lshr_b32 s4, s82, 2
	s_add_i32 s4, s4, s79
	s_mov_b64 vcc, s[0:1]
	s_cbranch_vccz .LBB1_26
	s_mul_hi_i32 s5, s4, 0x92492493
	s_add_i32 s5, s5, s4
	s_lshr_b32 s28, s5, 31
	s_ashr_i32 s5, s5, 12
	s_add_i32 s5, s5, s28
	s_mul_i32 s28, s5, 0x1c00
	s_sub_i32 s46, s4, s28
	s_bitcmp0_b32 s5, 0
	s_cselect_b32 s28, s16, 0x2a00
	s_ashr_i32 s49, s46, 1
	s_lshl_b32 s46, s46, 11
	s_add_i32 s28, s28, s49
	s_and_b32 s92, s46, 0x800
	s_cmp_lt_u32 s5, 2
	s_waitcnt lgkmcnt(0)
	s_cselect_b32 s50, s9, s11
	s_cselect_b32 s51, s8, s10
	s_lshl_b64 s[46:47], s[28:29], 14
	s_add_u32 s46, s51, s46
	s_addc_u32 s47, s50, s47
	s_lshl_b32 s93, s92, 2
	s_add_u32 s88, s46, s93
	s_addc_u32 s89, s47, 0
	s_lshl_b32 s5, s5, 6
	s_lshl_b32 s28, s28, 1
	s_and_b32 s46, s49, 0x7f
	s_and_b32 s5, s5, 0xffffff80
	s_and_b32 s28, s28, 0x7fffff00
	s_or_b32 s5, s5, s46
	s_add_i32 s46, s5, s28
	s_ashr_i32 s47, s46, 31
	s_lshl_b64 s[46:47], s[46:47], 13
	s_add_u32 s46, s14, s46
	s_addc_u32 s47, s15, s47
	s_lshl_b32 s93, s92, 1
	s_add_u32 s90, s46, s93
	s_addc_u32 s91, s47, 0
	s_branch .LBB1_12
.LBB1_11:
	s_ashr_i32 s5, s4, 31
	s_lshl_b64 s[4:5], s[4:5], 11
	s_waitcnt lgkmcnt(0)
	s_lshl_b64 s[88:89], s[4:5], 2
	s_add_u32 s88, s88, s12
	s_addc_u32 s89, s89, s13
	s_lshl_b64 s[90:91], s[4:5], 1
	s_add_u32 s90, s90, s26
	s_addc_u32 s91, s91, s27

.LBB1_14:
	ds_read_b128 v[148:151], v228
	ds_read_b128 v[152:155], v229
	ds_read_b128 v[156:159], v228 offset:2048
	ds_read_b128 v[160:163], v229 offset:2048
	s_add_i32 m0, s43, 0xc000
	ds_read_b128 v[132:135], v228 offset:16384
	ds_read_b128 v[136:139], v229 offset:16384
	ds_read_b128 v[140:143], v228 offset:18432
	ds_read_b128 v[144:147], v229 offset:18432
	ds_read_b128 v[166:169], v226
	ds_read_b128 v[170:173], v226 offset:2048
	ds_read_b128 v[174:177], v227
	ds_read_b128 v[178:181], v227 offset:2048
	ds_read_b128 v[182:185], v226 offset:4096
	ds_read_b128 v[186:189], v226 offset:6144
	ds_read_b128 v[190:193], v227 offset:4096
	ds_read_b128 v[214:217], v227 offset:6144
	global_load_lds_dwordx4 v208, s[44:45]
	s_add_i32 m0, s43, 0xe000
	s_nop 0
	global_load_lds_dwordx4 v210, s[44:45]
	s_waitcnt vmcnt(8)
	s_waitcnt lgkmcnt(0)
	s_barrier
	s_setprio 1
	s_waitcnt lgkmcnt(0)
	v_mfma_f32_16x16x32_f16 v[128:131], v[148:151], v[166:169], v[128:131]
	v_mfma_f32_16x16x32_f16 v[128:131], v[152:155], v[174:177], v[128:131]
	v_mfma_f32_16x16x32_f16 v[120:123], v[160:163], v[174:177], v[120:123]
	v_mfma_f32_16x16x32_f16 v[120:123], v[156:159], v[166:169], v[120:123]
	v_mfma_f32_16x16x32_f16 v[104:107], v[156:159], v[170:173], v[104:107]
	v_mfma_f32_16x16x32_f16 v[104:107], v[160:163], v[178:181], v[104:107]
	v_mfma_f32_16x16x32_f16 v[112:115], v[152:155], v[178:181], v[112:115]
	v_mfma_f32_16x16x32_f16 v[112:115], v[148:151], v[170:173], v[112:115]
	v_mfma_f32_16x16x32_f16 v[96:99], v[148:151], v[182:185], v[96:99]
	v_mfma_f32_16x16x32_f16 v[96:99], v[152:155], v[190:193], v[96:99]
	v_mfma_f32_16x16x32_f16 v[88:91], v[160:163], v[190:193], v[88:91]
	v_mfma_f32_16x16x32_f16 v[88:91], v[156:159], v[182:185], v[88:91]
	v_mfma_f32_16x16x32_f16 v[72:75], v[156:159], v[186:189], v[72:75]
	v_mfma_f32_16x16x32_f16 v[72:75], v[160:163], v[214:217], v[72:75]
	v_mfma_f32_16x16x32_f16 v[80:83], v[152:155], v[214:217], v[80:83]
	v_mfma_f32_16x16x32_f16 v[80:83], v[148:151], v[186:189], v[80:83]
	s_setprio 0
	s_setprio 1
	v_mfma_f32_16x16x32_f16 v[124:127], v[132:135], v[166:169], v[124:127]
	v_mfma_f32_16x16x32_f16 v[124:127], v[136:139], v[174:177], v[124:127]
	v_mfma_f32_16x16x32_f16 v[116:119], v[144:147], v[174:177], v[116:119]
	v_mfma_f32_16x16x32_f16 v[116:119], v[140:143], v[166:169], v[116:119]
	v_mfma_f32_16x16x32_f16 v[100:103], v[140:143], v[170:173], v[100:103]
	v_mfma_f32_16x16x32_f16 v[100:103], v[144:147], v[178:181], v[100:103]
	v_mfma_f32_16x16x32_f16 v[108:111], v[136:139], v[178:181], v[108:111]
	v_mfma_f32_16x16x32_f16 v[108:111], v[132:135], v[170:173], v[108:111]
	v_mfma_f32_16x16x32_f16 v[92:95], v[132:135], v[182:185], v[92:95]
	v_mfma_f32_16x16x32_f16 v[92:95], v[136:139], v[190:193], v[92:95]
	v_mfma_f32_16x16x32_f16 v[84:87], v[144:147], v[190:193], v[84:87]
	v_mfma_f32_16x16x32_f16 v[84:87], v[140:143], v[182:185], v[84:87]
	v_mfma_f32_16x16x32_f16 v[68:71], v[140:143], v[186:189], v[68:71]
	v_mfma_f32_16x16x32_f16 v[68:71], v[144:147], v[214:217], v[68:71]
	v_mfma_f32_16x16x32_f16 v[76:79], v[136:139], v[214:217], v[76:79]
	v_mfma_f32_16x16x32_f16 v[76:79], v[132:135], v[186:189], v[76:79]
	s_setprio 0
	s_barrier
	s_andn2_b64 vcc, exec, s[4:5]
	s_cbranch_vccnz .LBB1_16
	v_cvt_pkrtz_f16_f32 v166, v0, v1
	v_cvt_pkrtz_f16_f32 v167, v2, v3
	v_add_u32_e32 v166, 0x20002, v166
	v_add_u32_e32 v167, 0x20002, v167
	v_and_b32_e32 v166, 0xfffcfffc, v166
	v_and_b32_e32 v167, 0xfffcfffc, v167
	global_store_dwordx2 v231, v[166:167], s[90:91]

.LBB1_18:
	s_andn2_b64 vcc, exec, s[50:51]
	s_cbranch_vccnz .LBB1_20
	s_add_i32 m0, s43, 0x20000
	s_nop 0
	global_load_lds_dwordx4 v230, s[88:89]
	s_waitcnt vmcnt(9)

.LBB1_30:
	s_endpgm
	s_nop 0
	s_nop 0
	s_nop 0
	s_nop 0
	s_nop 0
	s_nop 0
	s_nop 0
	s_nop 0
	s_nop 0
	s_nop 0
	s_nop 0
	s_nop 0
	s_nop 0
	s_nop 0
	s_nop 0
	s_nop 0
	s_nop 0
	s_nop 0
	s_nop 0
	s_nop 0
	s_nop 0
	s_nop 0
	s_nop 0
	s_nop 0
	s_nop 0
	s_nop 0
	s_nop 0
	s_nop 0
	s_nop 0
	s_nop 0
	s_nop 0
	s_nop 0
	s_nop 0
	s_nop 0
	s_nop 0
	s_nop 0
	s_nop 0
	s_nop 0
	s_nop 0
	s_nop 0
	s_nop 0
	s_nop 0
	s_nop 0
	s_nop 0
	s_nop 0
	s_nop 0
	s_nop 0
	s_nop 0
	s_nop 0
	s_endpgm

	.amdhsa_kernel _Z12gemm_persistILi0ELi4096ELi32ELi112EEvPKDF16_S1_PvPKfS4_S4_S4_PDF16_S5_iii
		.amdhsa_group_segment_fixed_size 0
		.amdhsa_private_segment_fixed_size 0
		.amdhsa_kernarg_size 344
		.amdhsa_user_sgpr_count 2
		.amdhsa_user_sgpr_dispatch_ptr 0
		.amdhsa_user_sgpr_queue_ptr 0
		.amdhsa_user_sgpr_kernarg_segment_ptr 1
		.amdhsa_user_sgpr_dispatch_id 0
		.amdhsa_user_sgpr_kernarg_preload_length 0
		.amdhsa_user_sgpr_kernarg_preload_offset 0
		.amdhsa_user_sgpr_private_segment_size 0
		.amdhsa_uses_dynamic_stack 0
		.amdhsa_enable_private_segment 0
		.amdhsa_system_sgpr_workgroup_id_x 1
		.amdhsa_system_sgpr_workgroup_id_y 0
		.amdhsa_system_sgpr_workgroup_id_z 0
		.amdhsa_system_sgpr_workgroup_info 0
		.amdhsa_system_vgpr_workitem_id 0
		.amdhsa_next_free_vgpr 232
		.amdhsa_next_free_sgpr 94
		.amdhsa_accum_offset 232
		.amdhsa_reserve_vcc 1
		.amdhsa_float_round_mode_32 0
		.amdhsa_float_round_mode_16_64 0
		.amdhsa_float_denorm_mode_32 3
		.amdhsa_float_denorm_mode_16_64 3
		.amdhsa_dx10_clamp 1
		.amdhsa_ieee_mode 1
		.amdhsa_fp16_overflow 0
		.amdhsa_tg_split 0
		.amdhsa_exception_fp_ieee_invalid_op 0
		.amdhsa_exception_fp_denorm_src 0
		.amdhsa_exception_fp_ieee_div_zero 0
		.amdhsa_exception_fp_ieee_overflow 0
		.amdhsa_exception_fp_ieee_underflow 0
		.amdhsa_exception_fp_ieee_inexact 0
		.amdhsa_exception_int_div_zero 0
	.end_amdhsa_kernel

amdhsa.kernels:
  - .agpr_count:     4
    .args:
      - .actual_access:  read_only
        .address_space:  global
        .offset:         0
        .size:           8
        .value_kind:     global_buffer
      - .actual_access:  read_only
        .address_space:  global
        .offset:         8
        .size:           8
        .value_kind:     global_buffer
      - .actual_access:  read_only
        .address_space:  global
        .offset:         16
        .size:           8
        .value_kind:     global_buffer
      - .actual_access:  read_only
        .address_space:  global
        .offset:         24
        .size:           8
        .value_kind:     global_buffer
      - .actual_access:  write_only
        .address_space:  global
        .offset:         32
        .size:           8
        .value_kind:     global_buffer
      - .actual_access:  write_only
        .address_space:  global
        .offset:         40
        .size:           8
        .value_kind:     global_buffer
      - .actual_access:  write_only
        .address_space:  global
        .offset:         48
        .size:           8
        .value_kind:     global_buffer
    .group_segment_fixed_size: 4352
    .kernarg_segment_align: 8
    .kernarg_segment_size: 56
    .language:       OpenCL C
    .language_version:
      - 2
      - 0
    .max_flat_workgroup_size: 256
    .name:           _Z11prep_kernelPKfS0_S0_S0_PDF16_PfS1_
    .private_segment_fixed_size: 0
    .sgpr_count:     26
    .sgpr_spill_count: 0
    .symbol:         _Z11prep_kernelPKfS0_S0_S0_PDF16_PfS1_.kd
    .uniform_work_group_size: 1
    .uses_dynamic_stack: false
    .vgpr_count:     56
    .vgpr_spill_count: 0
    .wavefront_size: 64
  - .agpr_count:     0
    .args:
      - .address_space:  global
        .offset:         0
        .size:           8
        .value_kind:     global_buffer
      - .address_space:  global
        .offset:         8
        .size:           8
        .value_kind:     global_buffer
      - .actual_access:  write_only
        .address_space:  global
        .offset:         16
        .size:           8
        .value_kind:     global_buffer
      - .actual_access:  read_only
        .address_space:  global
        .offset:         24
        .size:           8
        .value_kind:     global_buffer
      - .address_space:  global
        .offset:         32
        .size:           8
        .value_kind:     global_buffer
      - .address_space:  global
        .offset:         40
        .size:           8
        .value_kind:     global_buffer
      - .address_space:  global
        .offset:         48
        .size:           8
        .value_kind:     global_buffer
      - .actual_access:  write_only
        .address_space:  global
        .offset:         56
        .size:           8
        .value_kind:     global_buffer
      - .actual_access:  write_only
        .address_space:  global
        .offset:         64
        .size:           8
        .value_kind:     global_buffer
      - .offset:         72
        .size:           4
        .value_kind:     by_value
      - .offset:         76
        .size:           4
        .value_kind:     by_value
      - .offset:         80
        .size:           4
        .value_kind:     by_value
      - .offset:         88
        .size:           4
        .value_kind:     hidden_block_count_x
      - .offset:         92
        .size:           4
        .value_kind:     hidden_block_count_y
      - .offset:         96
        .size:           4
        .value_kind:     hidden_block_count_z
      - .offset:         100
        .size:           2
        .value_kind:     hidden_group_size_x
      - .offset:         102
        .size:           2
        .value_kind:     hidden_group_size_y
      - .offset:         104
        .size:           2
        .value_kind:     hidden_group_size_z
      - .offset:         106
        .size:           2
        .value_kind:     hidden_remainder_x
      - .offset:         108
        .size:           2
        .value_kind:     hidden_remainder_y
      - .offset:         110
        .size:           2
        .value_kind:     hidden_remainder_z
      - .offset:         128
        .size:           8
        .value_kind:     hidden_global_offset_x
      - .offset:         136
        .size:           8
        .value_kind:     hidden_global_offset_y
      - .offset:         144
        .size:           8
        .value_kind:     hidden_global_offset_z
      - .offset:         152
        .size:           2
        .value_kind:     hidden_grid_dims
      - .offset:         208
        .size:           4
        .value_kind:     hidden_dynamic_lds_size
    .group_segment_fixed_size: 0
    .kernarg_segment_align: 8
    .kernarg_segment_size: 344
    .language:       OpenCL C
    .language_version:
      - 2
      - 0
    .max_flat_workgroup_size: 512
    .name:           _Z12gemm_persistILi0ELi4096ELi32ELi112EEvPKDF16_S1_PvPKfS4_S4_S4_PDF16_S5_iii
    .private_segment_fixed_size: 0
    .sgpr_count:     100
    .sgpr_spill_count: 0
    .symbol:         _Z12gemm_persistILi0ELi4096ELi32ELi112EEvPKDF16_S1_PvPKfS4_S4_S4_PDF16_S5_iii.kd
    .uniform_work_group_size: 1
    .uses_dynamic_stack: false
    .vgpr_count:     232
    .vgpr_spill_count: 0
    .wavefront_size: 64
  - .agpr_count:     0
    .args:
      - .address_space:  global
        .offset:         0
        .size:           8
        .value_kind:     global_buffer
      - .address_space:  global
        .offset:         8
        .size:           8
        .value_kind:     global_buffer
      - .actual_access:  write_only
        .address_space:  global
        .offset:         16
        .size:           8
        .value_kind:     global_buffer
      - .actual_access:  read_only
        .address_space:  global
        .offset:         24
        .size:           8
        .value_kind:     global_buffer
      - .actual_access:  read_only
        .address_space:  global
        .offset:         32
        .size:           8
        .value_kind:     global_buffer
      - .actual_access:  read_only
        .address_space:  global
        .offset:         40
        .size:           8
        .value_kind:     global_buffer
      - .actual_access:  read_only
        .address_space:  global
        .offset:         48
        .size:           8
        .value_kind:     global_buffer
      - .actual_access:  read_only
        .address_space:  global
        .offset:         56
        .size:           8
        .value_kind:     global_buffer
      - .actual_access:  read_only
        .address_space:  global
        .offset:         64
        .size:           8
        .value_kind:     global_buffer
      - .offset:         72
        .size:           4
        .value_kind:     by_value
      - .offset:         76
        .size:           4
        .value_kind:     by_value
      - .offset:         80
        .size:           4
        .value_kind:     by_value
      - .offset:         88
        .size:           4
        .value_kind:     hidden_block_count_x
      - .offset:         92
        .size:           4
        .value_kind:     hidden_block_count_y
      - .offset:         96
        .size:           4
        .value_kind:     hidden_block_count_z
      - .offset:         100
        .size:           2
        .value_kind:     hidden_group_size_x
      - .offset:         102
        .size:           2
        .value_kind:     hidden_group_size_y
      - .offset:         104
        .size:           2
        .value_kind:     hidden_group_size_z
      - .offset:         106
        .size:           2
        .value_kind:     hidden_remainder_x
      - .offset:         108
        .size:           2
        .value_kind:     hidden_remainder_y
      - .offset:         110
        .size:           2
        .value_kind:     hidden_remainder_z
      - .offset:         128
        .size:           8
        .value_kind:     hidden_global_offset_x
      - .offset:         136
        .size:           8
        .value_kind:     hidden_global_offset_y
      - .offset:         144
        .size:           8
        .value_kind:     hidden_global_offset_z
      - .offset:         152
        .size:           2
        .value_kind:     hidden_grid_dims
      - .offset:         208
        .size:           4
        .value_kind:     hidden_dynamic_lds_size
    .group_segment_fixed_size: 0
    .kernarg_segment_align: 8
    .kernarg_segment_size: 344
    .language:       OpenCL C
    .language_version:
      - 2
      - 0
    .max_flat_workgroup_size: 512
    .name:           _Z12gemm_persistILi1ELi14336ELi32ELi16EEvPKDF16_S1_PvPKfS4_S4_S4_PDF16_S5_iii
    .private_segment_fixed_size: 0
    .sgpr_count:     72
    .sgpr_spill_count: 0
    .symbol:         _Z12gemm_persistILi1ELi14336ELi32ELi16EEvPKDF16_S1_PvPKfS4_S4_S4_PDF16_S5_iii.kd
    .uniform_work_group_size: 1
    .uses_dynamic_stack: false
    .vgpr_count:     236
    .vgpr_spill_count: 0
    .wavefront_size: 64
